# GEMM2 scatter epilogue: dropped 128 canonicalizing v_max x,x feeding v_med3 clamps (value-identical)
# speedup vs baseline: 1.0061x; 1.0001x over previous
; __device__ __forceinline__ unsigned pk4_fp8(float a, float b, float c, float d) {
;     a = __builtin_fminf(__builtin_fmaxf(a, -448.f), 448.f); b = __builtin_fminf(__builtin_fmaxf(b, -448.f), 448.f); c = __builtin_fminf(__builtin_fmaxf(c, -448.f), 448.f); d = __builtin_fminf(__builtin_fmaxf(d, -448.f), 448.f);
;     int w = 0; w = __builtin_amdgcn_cvt_pk_fp8_f32(a, b, w, false); w = __builtin_amdgcn_cvt_pk_fp8_f32(c, d, w, true); return (unsigned)w; }
;     __device__ __forceinline__ void operator()(const f32x4 (&acc)[2][2][4][2], const Unit& u, int wr, int wc, int fr, int fq) const {
;     ...
;             for (int m = 0; m < 4; ++m) { const int rl = rl0 + ai * HALF + m * 16; if (rl < nv) {
;                 const f32x4 v00 = acc[ai][0][m][0] * sc, v01 = acc[ai][0][m][1] * sc, v10 = acc[ai][1][m][0] * sc, v11 = acc[ai][1][m][1] * sc;
;                 u32x4 w; w.x = pk4_fp8(v00[0], v00[1], v00[2], v00[3]); w.y = pk4_fp8(v01[0], v01[1], v01[2], v01[3]); w.z = pk4_fp8(v10[0], v10[1], v10[2], v10[3]); w.w = pk4_fp8(v11[0], v11[1], v11[2], v11[3]);
;                 __builtin_amdgcn_raw_buffer_store_b128(w, rs_, rl * ldc + col0, 0, 0); } }
.LBB0_1250:
	s_lshl_b32 s19, s19, 8
	s_lshl_b32 s20, s18, 1
	s_and_b32 s19, s19, 0x700
	s_add_i32 s20, s20, 0
	v_or_b32_e32 v36, s19, v206
	s_ashr_i32 s19, s18, 31
	s_add_i32 s20, s20, 0x20710
	v_mov_b32_e32 v37, s20
	s_lshl_b64 s[18:19], s[18:19], 19
	v_readlane_b32 s20, v254, 7
	s_add_u32 s20, s43, s18
	ds_read_u16 v37, v37
	v_readlane_b32 s21, v254, 8
	s_addc_u32 s18, s44, s19
	v_readlane_b32 s22, v254, 9
	v_readlane_b32 s23, v254, 10
	s_and_b32 s21, s18, 0xffff
	v_writelane_b32 v254, s20, 7
	s_waitcnt lgkmcnt(0)
	v_cmp_lt_i32_e32 vcc, v3, v37
	v_writelane_b32 v254, s21, 8
	v_writelane_b32 v254, s22, 9
	v_writelane_b32 v254, s23, 10
	s_and_saveexec_b64 s[18:19], vcc
	s_cbranch_execz .LBB0_1259
	v_med3_f32 v39, v184, s33, v214
	v_med3_f32 v40, v185, s33, v214
	v_med3_f32 v41, v182, s33, v214
	v_med3_f32 v42, v183, s33, v214
	v_mov_b32_e32 v38, v2
	v_cvt_pk_fp8_f32 v38, v39, v40
	v_med3_f32 v40, v180, s33, v214
	v_cvt_pk_fp8_f32 v38, v41, v42 op_sel:[0,0,1]
	v_med3_f32 v41, v181, s33, v214
	v_med3_f32 v42, v176, s33, v214
	v_med3_f32 v43, v177, s33, v214
	v_mov_b32_e32 v39, v2
	v_cvt_pk_fp8_f32 v39, v40, v41
	v_med3_f32 v41, v178, s33, v214
	v_cvt_pk_fp8_f32 v39, v42, v43 op_sel:[0,0,1]
	v_med3_f32 v42, v179, s33, v214
	v_med3_f32 v43, v174, s33, v214
	v_med3_f32 v44, v175, s33, v214
	v_mov_b32_e32 v40, v2
	v_cvt_pk_fp8_f32 v40, v41, v42
	v_med3_f32 v42, v162, s33, v214
	v_cvt_pk_fp8_f32 v40, v43, v44 op_sel:[0,0,1]
	v_med3_f32 v43, v163, s33, v214
	v_med3_f32 v44, v160, s33, v214
	v_med3_f32 v45, v161, s33, v214
	v_mov_b32_e32 v41, v2
	v_cvt_pk_fp8_f32 v41, v42, v43
	v_readlane_b32 s20, v254, 7
	v_or_b32_e32 v42, v36, v194
	v_readlane_b32 s21, v254, 8
	v_cvt_pk_fp8_f32 v41, v44, v45 op_sel:[0,0,1]
	v_readlane_b32 s22, v254, 9
	v_readlane_b32 s23, v254, 10
	s_nop 4
	buffer_store_dwordx4 v[38:41], v42, s[20:23], 0 offen
	s_or_b64 exec, exec, s[18:19]
	v_cmp_lt_i32_e32 vcc, v187, v37
	s_and_saveexec_b64 s[18:19], vcc
	s_cbranch_execnz .LBB0_1260

; __device__ __forceinline__ unsigned pk4_fp8(float a, float b, float c, float d) {
;     a = __builtin_fminf(__builtin_fmaxf(a, -448.f), 448.f); b = __builtin_fminf(__builtin_fmaxf(b, -448.f), 448.f); c = __builtin_fminf(__builtin_fmaxf(c, -448.f), 448.f); d = __builtin_fminf(__builtin_fmaxf(d, -448.f), 448.f);
;     int w = 0; w = __builtin_amdgcn_cvt_pk_fp8_f32(a, b, w, false); w = __builtin_amdgcn_cvt_pk_fp8_f32(c, d, w, true); return (unsigned)w; }
;     __device__ __forceinline__ void operator()(const f32x4 (&acc)[2][2][4][2], const Unit& u, int wr, int wc, int fr, int fq) const {
;     ...
;             for (int m = 0; m < 4; ++m) { const int rl = rl0 + ai * HALF + m * 16; if (rl < nv) {
;                 const f32x4 v00 = acc[ai][0][m][0] * sc, v01 = acc[ai][0][m][1] * sc, v10 = acc[ai][1][m][0] * sc, v11 = acc[ai][1][m][1] * sc;
;                 u32x4 w; w.x = pk4_fp8(v00[0], v00[1], v00[2], v00[3]); w.y = pk4_fp8(v01[0], v01[1], v01[2], v01[3]); w.z = pk4_fp8(v10[0], v10[1], v10[2], v10[3]); w.w = pk4_fp8(v11[0], v11[1], v11[2], v11[3]);
;                 __builtin_amdgcn_raw_buffer_store_b128(w, rs_, rl * ldc + col0, 0, 0); } }
.LBB0_1253:
	v_med3_f32 v39, v140, s33, v214
	v_med3_f32 v40, v141, s33, v214
	v_med3_f32 v41, v142, s33, v214
	v_med3_f32 v42, v143, s33, v214
	v_mov_b32_e32 v38, v2
	v_cvt_pk_fp8_f32 v38, v39, v40
	v_med3_f32 v40, v138, s33, v214
	v_cvt_pk_fp8_f32 v38, v41, v42 op_sel:[0,0,1]
	v_med3_f32 v41, v139, s33, v214
	v_med3_f32 v42, v134, s33, v214
	v_med3_f32 v43, v135, s33, v214
	v_mov_b32_e32 v39, v2
	v_cvt_pk_fp8_f32 v39, v40, v41
	v_med3_f32 v41, v136, s33, v214
	v_cvt_pk_fp8_f32 v39, v42, v43 op_sel:[0,0,1]
	v_med3_f32 v42, v137, s33, v214
	v_med3_f32 v43, v132, s33, v214
	v_med3_f32 v44, v133, s33, v214
	v_mov_b32_e32 v40, v2
	v_cvt_pk_fp8_f32 v40, v41, v42
	v_med3_f32 v42, v130, s33, v214
	v_cvt_pk_fp8_f32 v40, v43, v44 op_sel:[0,0,1]
	v_med3_f32 v43, v131, s33, v214
	v_med3_f32 v44, v128, s33, v214
	v_med3_f32 v45, v129, s33, v214
	v_mov_b32_e32 v41, v2
	v_cvt_pk_fp8_f32 v41, v42, v43
	v_readlane_b32 s20, v254, 7
	v_or_b32_e32 v42, v36, v196
	v_readlane_b32 s21, v254, 8
	v_cvt_pk_fp8_f32 v41, v44, v45 op_sel:[0,0,1]
	v_readlane_b32 s22, v254, 9
	v_readlane_b32 s23, v254, 10
	s_nop 4
	buffer_store_dwordx4 v[38:41], v42, s[20:23], 0 offen
	s_or_b64 exec, exec, s[18:19]
	v_cmp_lt_i32_e32 vcc, v189, v37
	s_and_saveexec_b64 s[18:19], vcc
	s_cbranch_execnz .LBB0_1262

; __device__ __forceinline__ unsigned pk4_fp8(float a, float b, float c, float d) {
;     a = __builtin_fminf(__builtin_fmaxf(a, -448.f), 448.f); b = __builtin_fminf(__builtin_fmaxf(b, -448.f), 448.f); c = __builtin_fminf(__builtin_fmaxf(c, -448.f), 448.f); d = __builtin_fminf(__builtin_fmaxf(d, -448.f), 448.f);
;     int w = 0; w = __builtin_amdgcn_cvt_pk_fp8_f32(a, b, w, false); w = __builtin_amdgcn_cvt_pk_fp8_f32(c, d, w, true); return (unsigned)w; }
;     __device__ __forceinline__ void operator()(const f32x4 (&acc)[2][2][4][2], const Unit& u, int wr, int wc, int fr, int fq) const {
;     ...
;             for (int m = 0; m < 4; ++m) { const int rl = rl0 + ai * HALF + m * 16; if (rl < nv) {
;                 const f32x4 v00 = acc[ai][0][m][0] * sc, v01 = acc[ai][0][m][1] * sc, v10 = acc[ai][1][m][0] * sc, v11 = acc[ai][1][m][1] * sc;
;                 u32x4 w; w.x = pk4_fp8(v00[0], v00[1], v00[2], v00[3]); w.y = pk4_fp8(v01[0], v01[1], v01[2], v01[3]); w.z = pk4_fp8(v10[0], v10[1], v10[2], v10[3]); w.w = pk4_fp8(v11[0], v11[1], v11[2], v11[3]);
;                 __builtin_amdgcn_raw_buffer_store_b128(w, rs_, rl * ldc + col0, 0, 0); } }
.LBB0_1255:
	v_med3_f32 v39, v106, s33, v214
	v_med3_f32 v40, v107, s33, v214
	v_med3_f32 v41, v104, s33, v214
	v_med3_f32 v42, v105, s33, v214
	v_mov_b32_e32 v38, v2
	v_cvt_pk_fp8_f32 v38, v39, v40
	v_med3_f32 v40, v102, s33, v214
	v_cvt_pk_fp8_f32 v38, v41, v42 op_sel:[0,0,1]
	v_med3_f32 v41, v103, s33, v214
	v_med3_f32 v42, v98, s33, v214
	v_med3_f32 v43, v99, s33, v214
	v_mov_b32_e32 v39, v2
	v_cvt_pk_fp8_f32 v39, v40, v41
	v_med3_f32 v41, v100, s33, v214
	v_cvt_pk_fp8_f32 v39, v42, v43 op_sel:[0,0,1]
	v_med3_f32 v42, v101, s33, v214
	v_med3_f32 v43, v96, s33, v214
	v_med3_f32 v44, v97, s33, v214
	v_mov_b32_e32 v40, v2
	v_cvt_pk_fp8_f32 v40, v41, v42
	v_med3_f32 v42, v94, s33, v214
	v_cvt_pk_fp8_f32 v40, v43, v44 op_sel:[0,0,1]
	v_med3_f32 v43, v95, s33, v214
	v_med3_f32 v44, v92, s33, v214
	v_med3_f32 v45, v93, s33, v214
	v_mov_b32_e32 v41, v2
	v_cvt_pk_fp8_f32 v41, v42, v43
	v_readlane_b32 s20, v254, 7
	v_or_b32_e32 v42, v36, v202
	v_readlane_b32 s21, v254, 8
	v_cvt_pk_fp8_f32 v41, v44, v45 op_sel:[0,0,1]
	v_readlane_b32 s22, v254, 9
	v_readlane_b32 s23, v254, 10
	s_nop 4
	buffer_store_dwordx4 v[38:41], v42, s[20:23], 0 offen
	s_or_b64 exec, exec, s[18:19]
	v_cmp_lt_i32_e32 vcc, v191, v37
	s_and_saveexec_b64 s[18:19], vcc
	s_cbranch_execnz .LBB0_1264

; __device__ __forceinline__ unsigned pk4_fp8(float a, float b, float c, float d) {
;     a = __builtin_fminf(__builtin_fmaxf(a, -448.f), 448.f); b = __builtin_fminf(__builtin_fmaxf(b, -448.f), 448.f); c = __builtin_fminf(__builtin_fmaxf(c, -448.f), 448.f); d = __builtin_fminf(__builtin_fmaxf(d, -448.f), 448.f);
;     int w = 0; w = __builtin_amdgcn_cvt_pk_fp8_f32(a, b, w, false); w = __builtin_amdgcn_cvt_pk_fp8_f32(c, d, w, true); return (unsigned)w; }
;     __device__ __forceinline__ void operator()(const f32x4 (&acc)[2][2][4][2], const Unit& u, int wr, int wc, int fr, int fq) const {
;     ...
;             for (int m = 0; m < 4; ++m) { const int rl = rl0 + ai * HALF + m * 16; if (rl < nv) {
;                 const f32x4 v00 = acc[ai][0][m][0] * sc, v01 = acc[ai][0][m][1] * sc, v10 = acc[ai][1][m][0] * sc, v11 = acc[ai][1][m][1] * sc;
;                 u32x4 w; w.x = pk4_fp8(v00[0], v00[1], v00[2], v00[3]); w.y = pk4_fp8(v01[0], v01[1], v01[2], v01[3]); w.z = pk4_fp8(v10[0], v10[1], v10[2], v10[3]); w.w = pk4_fp8(v11[0], v11[1], v11[2], v11[3]);
;                 __builtin_amdgcn_raw_buffer_store_b128(w, rs_, rl * ldc + col0, 0, 0); } }
.LBB0_1257:
	v_med3_f32 v38, v32, s33, v214
	v_med3_f32 v34, v34, s33, v214
	v_med3_f32 v35, v35, s33, v214
	v_med3_f32 v33, v33, s33, v214
	v_mov_b32_e32 v32, v2
	v_cvt_pk_fp8_f32 v32, v34, v35
	v_med3_f32 v30, v30, s33, v214
	v_cvt_pk_fp8_f32 v32, v38, v33 op_sel:[0,0,1]
	v_med3_f32 v31, v31, s33, v214
	v_mov_b32_e32 v33, v2
	v_cvt_pk_fp8_f32 v33, v30, v31
	v_med3_f32 v26, v26, s33, v214
	v_med3_f32 v27, v27, s33, v214
	v_cvt_pk_fp8_f32 v33, v26, v27 op_sel:[0,0,1]
	v_med3_f32 v26, v28, s33, v214
	v_med3_f32 v27, v29, s33, v214
	v_mov_b32_e32 v34, v2
	v_med3_f32 v22, v22, s33, v214
	v_med3_f32 v23, v23, s33, v214
	v_mov_b32_e32 v35, v2
	v_cvt_pk_fp8_f32 v34, v26, v27
	v_cvt_pk_fp8_f32 v35, v22, v23
	v_med3_f32 v24, v24, s33, v214
	v_med3_f32 v25, v25, s33, v214
	v_med3_f32 v20, v20, s33, v214
	v_med3_f32 v21, v21, s33, v214
	v_cvt_pk_fp8_f32 v34, v24, v25 op_sel:[0,0,1]
	v_cvt_pk_fp8_f32 v35, v20, v21 op_sel:[0,0,1]
	v_readlane_b32 s20, v254, 7
	v_or_b32_e32 v20, v36, v204
	v_readlane_b32 s21, v254, 8
	v_readlane_b32 s22, v254, 9
	v_readlane_b32 s23, v254, 10
	s_nop 4
	buffer_store_dwordx4 v[32:35], v20, s[20:23], 0 offen
	s_or_b64 exec, exec, s[18:19]
	v_cmp_lt_i32_e32 vcc, v193, v37
	s_and_saveexec_b64 s[18:19], vcc
	s_cbranch_execnz .LBB0_1266

; __device__ __forceinline__ unsigned pk4_fp8(float a, float b, float c, float d) {
;     a = __builtin_fminf(__builtin_fmaxf(a, -448.f), 448.f); b = __builtin_fminf(__builtin_fmaxf(b, -448.f), 448.f); c = __builtin_fminf(__builtin_fmaxf(c, -448.f), 448.f); d = __builtin_fminf(__builtin_fmaxf(d, -448.f), 448.f);
;     int w = 0; w = __builtin_amdgcn_cvt_pk_fp8_f32(a, b, w, false); w = __builtin_amdgcn_cvt_pk_fp8_f32(c, d, w, true); return (unsigned)w; }
;     __device__ __forceinline__ void operator()(const f32x4 (&acc)[2][2][4][2], const Unit& u, int wr, int wc, int fr, int fq) const {
;     ...
;             for (int m = 0; m < 4; ++m) { const int rl = rl0 + ai * HALF + m * 16; if (rl < nv) {
;                 const f32x4 v00 = acc[ai][0][m][0] * sc, v01 = acc[ai][0][m][1] * sc, v10 = acc[ai][1][m][0] * sc, v11 = acc[ai][1][m][1] * sc;
;                 u32x4 w; w.x = pk4_fp8(v00[0], v00[1], v00[2], v00[3]); w.y = pk4_fp8(v01[0], v01[1], v01[2], v01[3]); w.z = pk4_fp8(v10[0], v10[1], v10[2], v10[3]); w.w = pk4_fp8(v11[0], v11[1], v11[2], v11[3]);
;                 __builtin_amdgcn_raw_buffer_store_b128(w, rs_, rl * ldc + col0, 0, 0); } }
.LBB0_1260:
	v_med3_f32 v39, v158, s33, v214
	v_med3_f32 v40, v159, s33, v214
	v_med3_f32 v41, v156, s33, v214
	v_med3_f32 v42, v157, s33, v214
	v_mov_b32_e32 v38, v2
	v_cvt_pk_fp8_f32 v38, v39, v40
	v_med3_f32 v40, v154, s33, v214
	v_cvt_pk_fp8_f32 v38, v41, v42 op_sel:[0,0,1]
	v_med3_f32 v41, v155, s33, v214
	v_med3_f32 v42, v150, s33, v214
	v_med3_f32 v43, v151, s33, v214
	v_mov_b32_e32 v39, v2
	v_cvt_pk_fp8_f32 v39, v40, v41
	v_med3_f32 v41, v152, s33, v214
	v_cvt_pk_fp8_f32 v39, v42, v43 op_sel:[0,0,1]
	v_med3_f32 v42, v153, s33, v214
	v_med3_f32 v43, v148, s33, v214
	v_med3_f32 v44, v149, s33, v214
	v_mov_b32_e32 v40, v2
	v_cvt_pk_fp8_f32 v40, v41, v42
	v_med3_f32 v42, v146, s33, v214
	v_cvt_pk_fp8_f32 v40, v43, v44 op_sel:[0,0,1]
	v_med3_f32 v43, v147, s33, v214
	v_med3_f32 v44, v144, s33, v214
	v_med3_f32 v45, v145, s33, v214
	v_mov_b32_e32 v41, v2
	v_cvt_pk_fp8_f32 v41, v42, v43
	v_readlane_b32 s20, v254, 7
	v_or_b32_e32 v42, v36, v195
	v_readlane_b32 s21, v254, 8
	v_cvt_pk_fp8_f32 v41, v44, v45 op_sel:[0,0,1]
	v_readlane_b32 s22, v254, 9
	v_readlane_b32 s23, v254, 10
	s_nop 4
	buffer_store_dwordx4 v[38:41], v42, s[20:23], 0 offen
	s_or_b64 exec, exec, s[18:19]
	v_cmp_lt_i32_e32 vcc, v188, v37
	s_and_saveexec_b64 s[18:19], vcc
	s_cbranch_execnz .LBB0_1253

; __device__ __forceinline__ unsigned pk4_fp8(float a, float b, float c, float d) {
;     a = __builtin_fminf(__builtin_fmaxf(a, -448.f), 448.f); b = __builtin_fminf(__builtin_fmaxf(b, -448.f), 448.f); c = __builtin_fminf(__builtin_fmaxf(c, -448.f), 448.f); d = __builtin_fminf(__builtin_fmaxf(d, -448.f), 448.f);
;     int w = 0; w = __builtin_amdgcn_cvt_pk_fp8_f32(a, b, w, false); w = __builtin_amdgcn_cvt_pk_fp8_f32(c, d, w, true); return (unsigned)w; }
;     __device__ __forceinline__ void operator()(const f32x4 (&acc)[2][2][4][2], const Unit& u, int wr, int wc, int fr, int fq) const {
;     ...
;             for (int m = 0; m < 4; ++m) { const int rl = rl0 + ai * HALF + m * 16; if (rl < nv) {
;                 const f32x4 v00 = acc[ai][0][m][0] * sc, v01 = acc[ai][0][m][1] * sc, v10 = acc[ai][1][m][0] * sc, v11 = acc[ai][1][m][1] * sc;
;                 u32x4 w; w.x = pk4_fp8(v00[0], v00[1], v00[2], v00[3]); w.y = pk4_fp8(v01[0], v01[1], v01[2], v01[3]); w.z = pk4_fp8(v10[0], v10[1], v10[2], v10[3]); w.w = pk4_fp8(v11[0], v11[1], v11[2], v11[3]);
;                 __builtin_amdgcn_raw_buffer_store_b128(w, rs_, rl * ldc + col0, 0, 0); } }
.LBB0_1262:
	v_med3_f32 v39, v122, s33, v214
	v_med3_f32 v40, v123, s33, v214
	v_med3_f32 v41, v120, s33, v214
	v_med3_f32 v42, v121, s33, v214
	v_mov_b32_e32 v38, v2
	v_cvt_pk_fp8_f32 v38, v39, v40
	v_med3_f32 v40, v118, s33, v214
	v_cvt_pk_fp8_f32 v38, v41, v42 op_sel:[0,0,1]
	v_med3_f32 v41, v119, s33, v214
	v_med3_f32 v42, v114, s33, v214
	v_med3_f32 v43, v115, s33, v214
	v_mov_b32_e32 v39, v2
	v_cvt_pk_fp8_f32 v39, v40, v41
	v_med3_f32 v41, v116, s33, v214
	v_cvt_pk_fp8_f32 v39, v42, v43 op_sel:[0,0,1]
	v_med3_f32 v42, v117, s33, v214
	v_med3_f32 v43, v112, s33, v214
	v_med3_f32 v44, v113, s33, v214
	v_mov_b32_e32 v40, v2
	v_cvt_pk_fp8_f32 v40, v41, v42
	v_med3_f32 v42, v110, s33, v214
	v_cvt_pk_fp8_f32 v40, v43, v44 op_sel:[0,0,1]
	v_med3_f32 v43, v111, s33, v214
	v_med3_f32 v44, v108, s33, v214
	v_med3_f32 v45, v109, s33, v214
	v_mov_b32_e32 v41, v2
	v_cvt_pk_fp8_f32 v41, v42, v43
	v_readlane_b32 s20, v254, 7
	v_or_b32_e32 v42, v36, v197
	v_readlane_b32 s21, v254, 8
	v_cvt_pk_fp8_f32 v41, v44, v45 op_sel:[0,0,1]
	v_readlane_b32 s22, v254, 9
	v_readlane_b32 s23, v254, 10
	s_nop 4
	buffer_store_dwordx4 v[38:41], v42, s[20:23], 0 offen
	s_or_b64 exec, exec, s[18:19]
	v_cmp_lt_i32_e32 vcc, v190, v37
	s_and_saveexec_b64 s[18:19], vcc
	s_cbranch_execnz .LBB0_1255

; __device__ __forceinline__ unsigned pk4_fp8(float a, float b, float c, float d) {
;     a = __builtin_fminf(__builtin_fmaxf(a, -448.f), 448.f); b = __builtin_fminf(__builtin_fmaxf(b, -448.f), 448.f); c = __builtin_fminf(__builtin_fmaxf(c, -448.f), 448.f); d = __builtin_fminf(__builtin_fmaxf(d, -448.f), 448.f);
;     int w = 0; w = __builtin_amdgcn_cvt_pk_fp8_f32(a, b, w, false); w = __builtin_amdgcn_cvt_pk_fp8_f32(c, d, w, true); return (unsigned)w; }
;     __device__ __forceinline__ void operator()(const f32x4 (&acc)[2][2][4][2], const Unit& u, int wr, int wc, int fr, int fq) const {
;     ...
;             for (int m = 0; m < 4; ++m) { const int rl = rl0 + ai * HALF + m * 16; if (rl < nv) {
;                 const f32x4 v00 = acc[ai][0][m][0] * sc, v01 = acc[ai][0][m][1] * sc, v10 = acc[ai][1][m][0] * sc, v11 = acc[ai][1][m][1] * sc;
;                 u32x4 w; w.x = pk4_fp8(v00[0], v00[1], v00[2], v00[3]); w.y = pk4_fp8(v01[0], v01[1], v01[2], v01[3]); w.z = pk4_fp8(v10[0], v10[1], v10[2], v10[3]); w.w = pk4_fp8(v11[0], v11[1], v11[2], v11[3]);
;                 __builtin_amdgcn_raw_buffer_store_b128(w, rs_, rl * ldc + col0, 0, 0); } }
.LBB0_1264:
	v_med3_f32 v39, v82, s33, v214
	v_med3_f32 v40, v83, s33, v214
	v_med3_f32 v41, v80, s33, v214
	v_med3_f32 v42, v81, s33, v214
	v_mov_b32_e32 v38, v2
	v_cvt_pk_fp8_f32 v38, v39, v40
	v_med3_f32 v40, v74, s33, v214
	v_cvt_pk_fp8_f32 v38, v41, v42 op_sel:[0,0,1]
	v_med3_f32 v41, v75, s33, v214
	v_med3_f32 v42, v72, s33, v214
	v_med3_f32 v43, v73, s33, v214
	v_mov_b32_e32 v39, v2
	v_cvt_pk_fp8_f32 v39, v40, v41
	v_med3_f32 v41, v64, s33, v214
	v_cvt_pk_fp8_f32 v39, v42, v43 op_sel:[0,0,1]
	v_med3_f32 v42, v65, s33, v214
	v_med3_f32 v43, v66, s33, v214
	v_med3_f32 v44, v67, s33, v214
	v_mov_b32_e32 v40, v2
	v_cvt_pk_fp8_f32 v40, v41, v42
	v_med3_f32 v42, v56, s33, v214
	v_cvt_pk_fp8_f32 v40, v43, v44 op_sel:[0,0,1]
	v_med3_f32 v43, v57, s33, v214
	v_med3_f32 v44, v58, s33, v214
	v_med3_f32 v45, v59, s33, v214
	v_mov_b32_e32 v41, v2
	v_cvt_pk_fp8_f32 v41, v42, v43
	v_readlane_b32 s20, v254, 7
	v_or_b32_e32 v42, v36, v203
	v_readlane_b32 s21, v254, 8
	v_cvt_pk_fp8_f32 v41, v44, v45 op_sel:[0,0,1]
	v_readlane_b32 s22, v254, 9
	v_readlane_b32 s23, v254, 10
	s_nop 4
	buffer_store_dwordx4 v[38:41], v42, s[20:23], 0 offen
	s_or_b64 exec, exec, s[18:19]
	v_cmp_lt_i32_e32 vcc, v192, v37
	s_and_saveexec_b64 s[18:19], vcc
	s_cbranch_execnz .LBB0_1257

; __device__ __forceinline__ unsigned pk4_fp8(float a, float b, float c, float d) {
;     a = __builtin_fminf(__builtin_fmaxf(a, -448.f), 448.f); b = __builtin_fminf(__builtin_fmaxf(b, -448.f), 448.f); c = __builtin_fminf(__builtin_fmaxf(c, -448.f), 448.f); d = __builtin_fminf(__builtin_fmaxf(d, -448.f), 448.f);
;     int w = 0; w = __builtin_amdgcn_cvt_pk_fp8_f32(a, b, w, false); w = __builtin_amdgcn_cvt_pk_fp8_f32(c, d, w, true); return (unsigned)w; }
;     __device__ __forceinline__ void operator()(const f32x4 (&acc)[2][2][4][2], const Unit& u, int wr, int wc, int fr, int fq) const {
;     ...
;             for (int m = 0; m < 4; ++m) { const int rl = rl0 + ai * HALF + m * 16; if (rl < nv) {
;                 const f32x4 v00 = acc[ai][0][m][0] * sc, v01 = acc[ai][0][m][1] * sc, v10 = acc[ai][1][m][0] * sc, v11 = acc[ai][1][m][1] * sc;
;                 u32x4 w; w.x = pk4_fp8(v00[0], v00[1], v00[2], v00[3]); w.y = pk4_fp8(v01[0], v01[1], v01[2], v01[3]); w.z = pk4_fp8(v10[0], v10[1], v10[2], v10[3]); w.w = pk4_fp8(v11[0], v11[1], v11[2], v11[3]);
;                 __builtin_amdgcn_raw_buffer_store_b128(w, rs_, rl * ldc + col0, 0, 0); } }
.LBB0_1266:
	v_med3_f32 v20, v16, s33, v214
	v_med3_f32 v18, v18, s33, v214
	v_med3_f32 v19, v19, s33, v214
	v_med3_f32 v17, v17, s33, v214
	v_mov_b32_e32 v16, v2
	v_cvt_pk_fp8_f32 v16, v18, v19
	v_med3_f32 v14, v14, s33, v214
	v_cvt_pk_fp8_f32 v16, v20, v17 op_sel:[0,0,1]
	v_med3_f32 v15, v15, s33, v214
	v_mov_b32_e32 v17, v2
	v_cvt_pk_fp8_f32 v17, v14, v15
	v_med3_f32 v10, v10, s33, v214
	v_med3_f32 v11, v11, s33, v214
	v_cvt_pk_fp8_f32 v17, v10, v11 op_sel:[0,0,1]
	v_med3_f32 v10, v12, s33, v214
	v_med3_f32 v11, v13, s33, v214
	v_mov_b32_e32 v18, v2
	v_med3_f32 v6, v6, s33, v214
	v_med3_f32 v7, v7, s33, v214
	v_mov_b32_e32 v19, v2
	v_cvt_pk_fp8_f32 v18, v10, v11
	v_cvt_pk_fp8_f32 v19, v6, v7
	v_med3_f32 v8, v8, s33, v214
	v_med3_f32 v9, v9, s33, v214
	v_med3_f32 v4, v4, s33, v214
	v_med3_f32 v5, v5, s33, v214
	v_cvt_pk_fp8_f32 v18, v8, v9 op_sel:[0,0,1]
	v_cvt_pk_fp8_f32 v19, v4, v5 op_sel:[0,0,1]
	v_readlane_b32 s20, v254, 7
	v_or_b32_e32 v4, v36, v205
	v_readlane_b32 s21, v254, 8
	v_readlane_b32 s22, v254, 9
	v_readlane_b32 s23, v254, 10
	s_nop 4
	buffer_store_dwordx4 v[16:19], v4, s[20:23], 0 offen
	s_or_b64 exec, exec, s[18:19]
	s_and_b64 vcc, exec, s[2:3]
	s_mov_b64 s[2:3], -1
	s_cbranch_vccnz .LBB0_1237
